# u14 + the second half's 16 deferred exps executed before the mid-iteration barrier
# speedup vs baseline: 1.0248x; 1.0096x over previous
; template <bool FIRST> DEVI bool partialSM(f32x16& p0, f32x16& p1, float& m_reg, float& alpha) {
;     float pmax = p0[0];
; #pragma unroll
;     for (int r = 1; r < 16; ++r) pmax = fmaxf(pmax, p0[r]);
; #pragma unroll
;     for (int r = 0; r < 16; ++r) pmax = fmaxf(pmax, p1[r]);
;     { auto rr = __builtin_amdgcn_permlane32_swap(__float_as_uint(pmax), __float_as_uint(pmax), false, false);
;       pmax = fmaxf(__uint_as_float(rr[0]), __uint_as_float(rr[1])); }
;     if (FIRST) { m_reg = pmax; alpha = 1.f;
; #pragma unroll
;         for (int r = 0; r < 16; ++r) { p0[r] = __builtin_amdgcn_exp2f(p0[r] - pmax); p1[r] = p1[r] - pmax; }
;         return false;
;     } else if (__builtin_expect(__all(pmax <= ATT_THR), 1)) { alpha = 1.f;
; #pragma unroll
;         for (int r = 0; r < 16; ++r) p0[r] = __builtin_amdgcn_exp2f(p0[r]);
;         return false;
;     } else { const float d = fmaxf(pmax, 0.f); alpha = __builtin_amdgcn_exp2f(-d); m_reg += d;
; #pragma unroll
;         for (int r = 0; r < 16; ++r) { p0[r] = __builtin_amdgcn_exp2f(p0[r] - d); p1[r] = p1[r] - d; }
;         return true;
;     }
; }
; DEVI void finishSM(f32x16& p0, f32x16& p1, float alpha, float& l_reg, bf16x8& pa0, bf16x8& pa1, bf16x8& pa2, bf16x8& pa3) {
; #pragma unroll
;     for (int r = 0; r < 16; ++r) p1[r] = __builtin_amdgcn_exp2f(p1[r]);
;     f32x2 s2 = (f32x2){p0[0], p0[1]} + (f32x2){p1[0], p1[1]};
; #pragma unroll
;     for (int r = 2; r < 16; r += 2) s2 += (f32x2){p0[r], p0[r + 1]} + (f32x2){p1[r], p1[r + 1]};
;     float ps = s2[0] + s2[1];
;     { auto rr = __builtin_amdgcn_permlane32_swap(__float_as_uint(ps), __float_as_uint(ps), false, false);
;       ps = __uint_as_float(rr[0]) + __uint_as_float(rr[1]); }
;     l_reg = l_reg * alpha + ps;
;     ...
;     PK4(p0, 0, pa0); PK4(p0, 8, pa1); PK4(p1, 0, pa2); PK4(p1, 8, pa3);
;     ...
; }
; DEVI void qkt(f32x16& p0, f32x16& p1, const char* Kb, const bf16x8 (&qr)[6], int r32, int hi, const f32x16& cinit) {
; #pragma unroll
;     for (int d0 = 0; d0 < 6; ++d0) { const int cb = (d0 * 16 + hi * 8) * 2;
;         const bf16x8 k0 = *(const bf16x8*)(Kb + KSWZ(r32, cb)), k1 = *(const bf16x8*)(Kb + KSWZ(32 + r32, cb));
;         p0 = __builtin_amdgcn_mfma_f32_32x32x16_bf16(k0, qr[d0], d0 == 0 ? cinit : p0, 0, 0, 0);
;         p1 = __builtin_amdgcn_mfma_f32_32x32x16_bf16(k1, qr[d0], d0 == 0 ? cinit : p1, 0, 0, 0); }
; }
.LBB0_696:
	v_add_u32_e32 v174, s98, v204
	v_exp_f32_e32 v66, v66
	v_exp_f32_e32 v67, v67
	s_waitcnt lgkmcnt(1)
	v_mfma_f32_32x32x16_bf16 v[98:113], v[82:85], v[150:153], v[34:49]
	v_add_u32_e32 v82, s98, v184
	v_add_u32_e32 v83, s98, v185
	ds_read_b128 v[208:211], v82 offset:12288
	ds_read_b128 v[212:215], v82 offset:18432
	ds_read_b128 v[216:219], v83 offset:12288
	ds_read_b128 v[220:223], v83 offset:18432
	v_exp_f32_e32 v68, v68
	v_exp_f32_e32 v69, v69
	v_exp_f32_e32 v70, v70
	v_exp_f32_e32 v71, v71
	s_waitcnt lgkmcnt(4)
	v_mfma_f32_32x32x16_bf16 v[82:97], v[124:127], v[150:153], v[34:49]
	ds_read_b128 v[124:127], v174 offset:12288
	ds_read_b128 v[224:227], v174 offset:18432
	v_exp_f32_e32 v72, v72
	v_exp_f32_e32 v73, v73
	v_exp_f32_e32 v74, v74
	v_exp_f32_e32 v75, v75
	v_exp_f32_e32 v76, v76
	v_exp_f32_e32 v77, v77
	s_waitcnt lgkmcnt(5)
	v_mfma_f32_32x32x16_bf16 v[98:113], v[208:211], v[138:141], v[98:113]
	v_add_u32_e32 v174, s98, v205
	v_exp_f32_e32 v78, v78
	v_exp_f32_e32 v79, v79
	ds_read_b128 v[228:231], v174 offset:12288
	ds_read_b128 v[232:235], v174 offset:18432
	v_exp_f32_e32 v80, v80
	v_exp_f32_e32 v81, v81
	v_add_u32_e32 v174, s98, v206
	s_waitcnt lgkmcnt(6)
	v_mfma_f32_32x32x16_bf16 v[82:97], v[212:215], v[138:141], v[82:97]
	v_add_f32_e64 v212, v50, v66
	v_add_f32_e64 v213, v51, v67
	v_add_f32_e64 v214, v52, v68
	v_add_f32_e64 v215, v53, v69
	v_lshl_add_u32 v202, s89, 14, v115
	v_add_f32_e32 v212, v214, v212
	v_add_f32_e32 v213, v215, v213
	v_add_f32_e32 v214, v54, v70
	v_add_f32_e32 v215, v55, v71
	ds_read_b128 v[208:211], v174 offset:12288
	ds_read_b128 v[236:239], v174 offset:18432
	v_add_f32_e32 v212, v214, v212
	v_add_f32_e32 v213, v215, v213
	s_waitcnt lgkmcnt(7)
	v_mfma_f32_32x32x16_bf16 v[98:113], v[216:219], v[134:137], v[98:113]
	v_add_f32_e64 v214, v56, v72
	v_add_f32_e64 v215, v57, v73
	v_cvt_pk_bf16_f32 v50, v50, v51
	v_cvt_pk_bf16_f32 v51, v52, v53
	v_cvt_pk_bf16_f32 v52, v54, v55
	v_cvt_pk_bf16_f32 v53, v56, v57
	v_cvt_pk_bf16_f32 v54, v58, v59
	v_add_f32_e64 v212, v214, v212
	v_add_f32_e64 v213, v215, v213
	s_waitcnt lgkmcnt(6)
	v_mfma_f32_32x32x16_bf16 v[82:97], v[220:223], v[134:137], v[82:97]
	v_add_f32_e64 v214, v58, v74
	v_add_f32_e64 v215, v59, v75
	v_cvt_pk_bf16_f32 v55, v60, v61
	v_cvt_pk_bf16_f32 v56, v62, v63
	v_cvt_pk_bf16_f32 v57, v64, v65
	v_cvt_pk_bf16_f32 v58, v66, v67
	v_cvt_pk_bf16_f32 v59, v68, v69
	v_add_f32_e64 v212, v214, v212
	v_add_f32_e64 v213, v215, v213
	s_waitcnt lgkmcnt(5)
	v_mfma_f32_32x32x16_bf16 v[98:113], v[124:127], v[130:133], v[98:113]
	v_add_f32_e64 v214, v60, v76
	v_add_f32_e64 v215, v61, v77
	v_add_f32_e64 v126, v62, v78
	v_add_f32_e64 v127, v63, v79
	v_add_f32_e64 v124, v214, v212
	v_add_f32_e64 v125, v215, v213
	v_cvt_pk_bf16_f32 v60, v70, v71
	v_cvt_pk_bf16_f32 v61, v72, v73
	v_cvt_pk_bf16_f32 v62, v74, v75
	v_cvt_pk_bf16_f32 v63, v76, v77
	s_waitcnt lgkmcnt(4)
	v_mfma_f32_32x32x16_bf16 v[82:97], v[224:227], v[130:133], v[82:97]
	v_add_f32_e64 v124, v126, v124
	v_add_f32_e64 v125, v127, v125
	v_add_f32_e64 v126, v64, v80
	v_add_f32_e64 v127, v65, v81
	v_cvt_pk_bf16_f32 v64, v78, v79
	v_cvt_pk_bf16_f32 v65, v80, v81
	ds_read_b64_tr_b16 v[66:67], v202 offset:0
	ds_read_b64_tr_b16 v[68:69], v202 offset:0x400
	ds_read_b64_tr_b16 v[70:71], v202 offset:0x800
	s_waitcnt lgkmcnt(6)
	v_mfma_f32_32x32x16_bf16 v[98:113], v[228:231], v[146:149], v[98:113]
	ds_read_b64_tr_b16 v[72:73], v202 offset:0xc00
	ds_read_b64_tr_b16 v[74:75], v202 offset:0x1000
	ds_read_b64_tr_b16 v[76:77], v202 offset:0x1400
	ds_read_b64_tr_b16 v[78:79], v202 offset:0x1800
	ds_read_b64_tr_b16 v[80:81], v202 offset:0x1c00
	v_add_f32_e64 v124, v126, v124
	v_add_f32_e64 v125, v127, v125
	s_waitcnt lgkmcnt(10)
	v_mfma_f32_32x32x16_bf16 v[82:97], v[232:235], v[146:149], v[82:97]
	v_add_f32_e32 v124, v124, v125
	s_nop 0
	v_mov_b32_e32 v125, v124
	s_nop 1
	v_permlane32_swap_b32_e32 v124, v125
	s_waitcnt lgkmcnt(9)
	v_mfma_f32_32x32x16_bf16 v[98:113], v[208:211], v[142:145], v[98:113]
	ds_read_b64_tr_b16 v[208:209], v202 offset:0x200
	ds_read_b64_tr_b16 v[210:211], v202 offset:0x600
	ds_read_b64_tr_b16 v[212:213], v202 offset:0xa00
	ds_read_b64_tr_b16 v[214:215], v202 offset:0xe00
	ds_read_b64_tr_b16 v[216:217], v202 offset:0x1200
	ds_read_b64_tr_b16 v[218:219], v202 offset:0x1600
	ds_read_b64_tr_b16 v[220:221], v202 offset:0x1a00
	s_waitcnt lgkmcnt(15)
	v_mfma_f32_32x32x16_bf16 v[82:97], v[236:239], v[142:145], v[82:97]
	ds_read_b64_tr_b16 v[222:223], v202 offset:0x1e00
	s_waitcnt lgkmcnt(14)
	v_mfma_f32_32x32x16_bf16 v[18:33], v[50:53], v[66:69], v[18:33]
	s_waitcnt lgkmcnt(6)
	v_mfma_f32_32x32x16_bf16 v[2:17], v[50:53], v[208:211], v[2:17]
	s_nop 8
	v_max_f32_e32 v249, v99, v99
	v_max_f32_e32 v250, v98, v98
	v_max_f32_e32 v249, v250, v249
	v_max3_f32 v249, v249, v100, v101
	v_max3_f32 v249, v249, v102, v103
	v_max3_f32 v251, v249, v104, v105
	v_max3_f32 v251, v251, v106, v107
	v_exp_f32_e32 v50, v98
	v_exp_f32_e32 v51, v99
	v_exp_f32_e32 v52, v100
	v_exp_f32_e32 v53, v101
	v_mfma_f32_32x32x16_bf16 v[18:33], v[54:57], v[70:73], v[18:33]
	s_waitcnt lgkmcnt(4)
	v_mfma_f32_32x32x16_bf16 v[2:17], v[54:57], v[212:215], v[2:17]
	v_max3_f32 v251, v251, v108, v109
	v_max3_f32 v251, v251, v110, v111
	v_max3_f32 v251, v251, v112, v113
	v_max3_f32 v251, v251, v82, v83
	v_max3_f32 v251, v251, v84, v85
	v_max3_f32 v251, v251, v86, v87
	v_max3_f32 v251, v251, v88, v89
	v_exp_f32_e32 v54, v102
	v_exp_f32_e32 v55, v103
	v_exp_f32_e32 v56, v104
	v_exp_f32_e32 v57, v105
	v_mfma_f32_32x32x16_bf16 v[18:33], v[58:61], v[74:77], v[18:33]
	s_waitcnt lgkmcnt(2)
	v_mfma_f32_32x32x16_bf16 v[2:17], v[58:61], v[216:219], v[2:17]
	v_max3_f32 v251, v251, v90, v91
	v_max3_f32 v251, v251, v92, v93
	v_max3_f32 v251, v251, v94, v95
	v_max3_f32 v251, v251, v96, v97
	v_mov_b32_e32 v252, v251
	s_nop 1
	v_permlane32_swap_b32_e32 v251, v252
	v_exp_f32_e32 v58, v106
	v_exp_f32_e32 v59, v107
	v_exp_f32_e32 v60, v108
	v_exp_f32_e32 v61, v109
	v_mfma_f32_32x32x16_bf16 v[18:33], v[62:65], v[78:81], v[18:33]
	s_waitcnt lgkmcnt(0)
	v_mfma_f32_32x32x16_bf16 v[2:17], v[62:65], v[220:223], v[2:17]
	v_exp_f32_e32 v62, v110
	v_exp_f32_e32 v63, v111
	v_exp_f32_e32 v64, v112
	v_exp_f32_e32 v65, v113
	v_max_f32_e32 v252, v252, v252
	v_max_f32_e32 v251, v251, v251
	v_max_f32_e32 v126, v251, v252
	v_cmp_ge_f32_e32 vcc, s79, v126
	s_cmp_lg_u64 vcc, exec
	s_cselect_b64 s[6:7], -1, 0
	s_cbranch_scc1 .LBB0_705
	v_mov_b32_e32 v208, 1.0
	v_mov_b32_e32 v209, v203
	v_exp_f32_e32 v82, v82
	v_exp_f32_e32 v83, v83
	v_exp_f32_e32 v84, v84
	v_exp_f32_e32 v85, v85
	v_exp_f32_e32 v86, v86
	v_exp_f32_e32 v87, v87
	v_exp_f32_e32 v88, v88
	v_exp_f32_e32 v89, v89
	v_exp_f32_e32 v90, v90
	v_exp_f32_e32 v91, v91
	v_exp_f32_e32 v92, v92
	v_exp_f32_e32 v93, v93
	v_exp_f32_e32 v94, v94
	v_exp_f32_e32 v95, v95
	v_exp_f32_e32 v96, v96
	v_exp_f32_e32 v97, v97
	s_branch .LBB0_699

; template <bool FIRST> DEVI bool partialSM(f32x16& p0, f32x16& p1, float& m_reg, float& alpha) {
;     float pmax = p0[0];
; #pragma unroll
;     for (int r = 1; r < 16; ++r) pmax = fmaxf(pmax, p0[r]);
; #pragma unroll
;     for (int r = 0; r < 16; ++r) pmax = fmaxf(pmax, p1[r]);
;     { auto rr = __builtin_amdgcn_permlane32_swap(__float_as_uint(pmax), __float_as_uint(pmax), false, false);
;       pmax = fmaxf(__uint_as_float(rr[0]), __uint_as_float(rr[1])); }
;     if (FIRST) { m_reg = pmax; alpha = 1.f;
; #pragma unroll
;         for (int r = 0; r < 16; ++r) { p0[r] = __builtin_amdgcn_exp2f(p0[r] - pmax); p1[r] = p1[r] - pmax; }
;         return false;
;     } else if (__builtin_expect(__all(pmax <= ATT_THR), 1)) { alpha = 1.f;
; #pragma unroll
;         for (int r = 0; r < 16; ++r) p0[r] = __builtin_amdgcn_exp2f(p0[r]);
;         return false;
;     } else { const float d = fmaxf(pmax, 0.f); alpha = __builtin_amdgcn_exp2f(-d); m_reg += d;
; #pragma unroll
;         for (int r = 0; r < 16; ++r) { p0[r] = __builtin_amdgcn_exp2f(p0[r] - d); p1[r] = p1[r] - d; }
;         return true;
;     }
; }
; DEVI void finishSM(f32x16& p0, f32x16& p1, float alpha, float& l_reg, bf16x8& pa0, bf16x8& pa1, bf16x8& pa2, bf16x8& pa3) {
; #pragma unroll
;     for (int r = 0; r < 16; ++r) p1[r] = __builtin_amdgcn_exp2f(p1[r]);
;     f32x2 s2 = (f32x2){p0[0], p0[1]} + (f32x2){p1[0], p1[1]};
; #pragma unroll
;     for (int r = 2; r < 16; r += 2) s2 += (f32x2){p0[r], p0[r + 1]} + (f32x2){p1[r], p1[r + 1]};
;     float ps = s2[0] + s2[1];
;     { auto rr = __builtin_amdgcn_permlane32_swap(__float_as_uint(ps), __float_as_uint(ps), false, false);
;       ps = __uint_as_float(rr[0]) + __uint_as_float(rr[1]); }
;     l_reg = l_reg * alpha + ps;
;     ...
;     PK4(p0, 0, pa0); PK4(p0, 8, pa1); PK4(p1, 0, pa2); PK4(p1, 8, pa3);
;     ...
; }
; DEVI void qkt(f32x16& p0, f32x16& p1, const char* Kb, const bf16x8 (&qr)[6], int r32, int hi, const f32x16& cinit) {
; #pragma unroll
;     for (int d0 = 0; d0 < 6; ++d0) { const int cb = (d0 * 16 + hi * 8) * 2;
;         const bf16x8 k0 = *(const bf16x8*)(Kb + KSWZ(r32, cb)), k1 = *(const bf16x8*)(Kb + KSWZ(32 + r32, cb));
;         p0 = __builtin_amdgcn_mfma_f32_32x32x16_bf16(k0, qr[d0], d0 == 0 ? cinit : p0, 0, 0, 0);
;         p1 = __builtin_amdgcn_mfma_f32_32x32x16_bf16(k1, qr[d0], d0 == 0 ? cinit : p1, 0, 0, 0); }
; }
.LBB0_702:
	s_mul_i32 s98, s2, 0x6000
	s_add_i32 s98, s96, s98
	s_lshl_b32 s99, s2, 14
	s_add_i32 s99, s97, s99
	s_mul_i32 s6, s61, 0x6000
	s_add_i32 s6, s6, 0
	v_add_u32_e32 v249, s6, v129
	v_lshl_add_u64 v[250:251], v[118:119], 0, s[12:13]
	s_mov_b32 m0, s98
	s_barrier
	ds_read_b128 v[234:237], v249
	ds_read_b128 v[210:213], v249 offset:6144
	global_load_lds_dwordx4 v[250:251], off
	s_waitcnt lgkmcnt(1)
	v_mfma_f32_32x32x16_bf16 v[98:113], v[234:237], v[150:153], v[34:49]
	v_add_u32_e32 v126, s6, v184
	v_lshl_add_u64 v[250:251], v[120:121], 0, s[12:13]
	s_add_i32 m0, s98, 0x2000
	global_load_lds_dwordx4 v[250:251], off
	s_waitcnt lgkmcnt(0)
	v_mfma_f32_32x32x16_bf16 v[66:81], v[210:213], v[150:153], v[34:49]
	ds_read_b128 v[210:213], v126
	ds_read_b128 v[214:217], v126 offset:6144
	v_add_u32_e32 v126, s6, v185
	v_lshl_add_u64 v[250:251], v[122:123], 0, s[12:13]
	s_add_i32 m0, s98, 0x4000
	global_load_lds_dwordx4 v[250:251], off
	s_waitcnt lgkmcnt(1)
	v_mfma_f32_32x32x16_bf16 v[98:113], v[210:213], v[138:141], v[98:113]
	s_mov_b32 m0, s99
	v_lshl_add_u64 v[250:251], v[116:117], 0, s[40:41]
	global_load_lds_dwordx4 v[116:117], off
	s_add_i32 m0, s99, 0x2000
	v_add_u32_e32 v174, 0x2000, v202
	global_load_lds_dwordx4 v[250:251], off
	s_waitcnt lgkmcnt(0)
	v_mfma_f32_32x32x16_bf16 v[66:81], v[214:217], v[138:141], v[66:81]
	ds_read_b128 v[210:213], v126
	ds_read_b128 v[214:217], v126 offset:6144
	v_add_u32_e32 v126, s6, v204
	s_waitcnt lgkmcnt(1)
	v_mfma_f32_32x32x16_bf16 v[98:113], v[210:213], v[134:137], v[98:113]
	ds_read_b128 v[210:213], v126
	ds_read_b128 v[218:221], v126 offset:6144
	v_add_u32_e32 v126, s6, v205
	s_waitcnt lgkmcnt(2)
	v_mfma_f32_32x32x16_bf16 v[66:81], v[214:217], v[134:137], v[66:81]
	ds_read_b128 v[214:217], v126
	ds_read_b128 v[222:225], v126 offset:6144
	v_add_u32_e32 v126, s6, v206
	ds_read_b128 v[226:229], v126
	ds_read_b128 v[230:233], v126 offset:6144
	v_add_f32_e32 v126, v50, v82
	v_add_f32_e32 v127, v51, v83
	v_cvt_pk_bf16_f32 v50, v50, v51
	v_cvt_pk_bf16_f32 v51, v52, v53
	s_waitcnt lgkmcnt(5)
	v_mfma_f32_32x32x16_bf16 v[98:113], v[210:213], v[130:133], v[98:113]
	v_add_f32_e64 v210, v52, v84
	v_add_f32_e64 v211, v53, v85
	v_cvt_pk_bf16_f32 v52, v54, v55
	v_cvt_pk_bf16_f32 v53, v56, v57
	v_add_f32_e64 v126, v210, v126
	v_add_f32_e64 v127, v211, v127
	v_add_f32_e64 v210, v54, v86
	v_add_f32_e64 v211, v55, v87
	v_cvt_pk_bf16_f32 v54, v58, v59
	s_waitcnt lgkmcnt(4)
	v_mfma_f32_32x32x16_bf16 v[66:81], v[218:221], v[130:133], v[66:81]
	v_add_f32_e64 v126, v210, v126
	v_add_f32_e64 v127, v211, v127
	v_add_f32_e64 v210, v56, v88
	v_add_f32_e64 v211, v57, v89
	v_cvt_pk_bf16_f32 v55, v60, v61
	v_cvt_pk_bf16_f32 v56, v62, v63
	v_cvt_pk_bf16_f32 v57, v64, v65
	v_add_f32_e64 v126, v210, v126
	v_add_f32_e64 v127, v211, v127
	v_add_f32_e32 v210, v58, v90
	v_add_f32_e32 v211, v59, v91
	v_cvt_pk_bf16_f32 v58, v82, v83
	v_cvt_pk_bf16_f32 v59, v84, v85
	s_waitcnt lgkmcnt(3)
	v_mfma_f32_32x32x16_bf16 v[98:113], v[214:217], v[146:149], v[98:113]
	v_add_f32_e64 v126, v210, v126
	v_add_f32_e64 v127, v211, v127
	v_add_f32_e64 v210, v60, v92
	v_add_f32_e64 v211, v61, v93
	v_cvt_pk_bf16_f32 v60, v86, v87
	v_cvt_pk_bf16_f32 v61, v88, v89
	v_add_f32_e64 v126, v210, v126
	v_add_f32_e64 v127, v211, v127
	v_add_f32_e32 v210, v62, v94
	v_add_f32_e32 v211, v63, v95
	v_cvt_pk_bf16_f32 v62, v90, v91
	v_cvt_pk_bf16_f32 v63, v92, v93
	s_waitcnt lgkmcnt(2)
	v_mfma_f32_32x32x16_bf16 v[66:81], v[222:225], v[146:149], v[66:81]
	v_add_f32_e64 v126, v210, v126
	v_add_f32_e64 v127, v211, v127
	v_add_f32_e64 v210, v64, v96
	v_add_f32_e64 v211, v65, v97
	v_cvt_pk_bf16_f32 v64, v94, v95
	v_cvt_pk_bf16_f32 v65, v96, v97
	ds_read_b64_tr_b16 v[154:155], v174 offset:0
	ds_read_b64_tr_b16 v[156:157], v174 offset:0x400
	ds_read_b64_tr_b16 v[158:159], v174 offset:0x800
	ds_read_b64_tr_b16 v[160:161], v174 offset:0xc00
	ds_read_b64_tr_b16 v[162:163], v174 offset:0x1000
	ds_read_b64_tr_b16 v[164:165], v174 offset:0x1400
	ds_read_b64_tr_b16 v[166:167], v174 offset:0x1800
	ds_read_b64_tr_b16 v[168:169], v174 offset:0x1c00
	v_add_f32_e64 v126, v210, v126
	v_add_f32_e64 v127, v211, v127
	ds_read_b64_tr_b16 v[210:211], v174 offset:0x200
	ds_read_b64_tr_b16 v[212:213], v174 offset:0x600
	ds_read_b64_tr_b16 v[214:215], v174 offset:0xa00
	s_waitcnt lgkmcnt(12)
	v_mfma_f32_32x32x16_bf16 v[98:113], v[226:229], v[142:145], v[98:113]
	ds_read_b64_tr_b16 v[216:217], v174 offset:0xe00
	ds_read_b64_tr_b16 v[218:219], v174 offset:0x1200
	ds_read_b64_tr_b16 v[220:221], v174 offset:0x1600
	ds_read_b64_tr_b16 v[222:223], v174 offset:0x1a00
	ds_read_b64_tr_b16 v[224:225], v174 offset:0x1e00
	v_add_f32_e32 v126, v126, v127
	s_waitcnt lgkmcnt(15)
	v_mfma_f32_32x32x16_bf16 v[66:81], v[230:233], v[142:145], v[66:81]
	v_mov_b32_e32 v127, v126
	s_nop 1
	v_permlane32_swap_b32_e32 v126, v127
	s_waitcnt lgkmcnt(14)
	v_mfma_f32_32x32x16_bf16 v[18:33], v[50:53], v[154:157], v[18:33]
	s_waitcnt lgkmcnt(6)
	v_mfma_f32_32x32x16_bf16 v[2:17], v[50:53], v[210:213], v[2:17]
	s_nop 4
	v_max_f32_e32 v249, v99, v99
	v_max_f32_e32 v250, v98, v98
	v_max_f32_e32 v249, v250, v249
	v_max3_f32 v249, v249, v100, v101
	v_max3_f32 v249, v249, v102, v103
	v_max3_f32 v251, v249, v104, v105
	v_max3_f32 v251, v251, v106, v107
	v_exp_f32_e32 v50, v98
	v_exp_f32_e32 v51, v99
	v_exp_f32_e32 v52, v100
	v_exp_f32_e32 v53, v101
	v_mfma_f32_32x32x16_bf16 v[18:33], v[54:57], v[158:161], v[18:33]
	s_waitcnt lgkmcnt(4)
	v_mfma_f32_32x32x16_bf16 v[2:17], v[54:57], v[214:217], v[2:17]
	v_max3_f32 v251, v251, v108, v109
	v_max3_f32 v251, v251, v110, v111
	v_max3_f32 v251, v251, v112, v113
	v_max3_f32 v251, v251, v66, v67
	v_max3_f32 v251, v251, v68, v69
	v_max3_f32 v251, v251, v70, v71
	v_max3_f32 v251, v251, v72, v73
	v_exp_f32_e32 v54, v102
	v_exp_f32_e32 v55, v103
	v_exp_f32_e32 v56, v104
	v_exp_f32_e32 v57, v105
	v_mfma_f32_32x32x16_bf16 v[18:33], v[58:61], v[162:165], v[18:33]
	s_waitcnt lgkmcnt(2)
	v_mfma_f32_32x32x16_bf16 v[2:17], v[58:61], v[218:221], v[2:17]
	v_max3_f32 v251, v251, v74, v75
	v_max3_f32 v251, v251, v76, v77
	v_max3_f32 v251, v251, v78, v79
	v_max3_f32 v251, v251, v80, v81
	v_mov_b32_e32 v252, v251
	s_nop 1
	v_permlane32_swap_b32_e32 v251, v252
	v_exp_f32_e32 v58, v106
	v_exp_f32_e32 v59, v107
	v_exp_f32_e32 v60, v108
	v_exp_f32_e32 v61, v109
	v_mfma_f32_32x32x16_bf16 v[18:33], v[62:65], v[166:169], v[18:33]
	s_waitcnt lgkmcnt(0)
	v_mfma_f32_32x32x16_bf16 v[2:17], v[62:65], v[222:225], v[2:17]
	v_exp_f32_e32 v62, v110
	v_exp_f32_e32 v63, v111
	v_exp_f32_e32 v64, v112
	v_exp_f32_e32 v65, v113
	v_max_f32_e32 v252, v252, v252
	v_max_f32_e32 v251, v251, v251
	v_max_f32_e32 v174, v251, v252
	v_cmp_ge_f32_e32 vcc, s79, v174
	s_cmp_lg_u64 vcc, exec
	s_cselect_b64 s[6:7], -1, 0
	s_cbranch_scc1 .LBB0_711
	v_mov_b32_e32 v202, 1.0
	v_mov_b32_e32 v203, v209
	s_branch .LBB0_716

; template <bool FIRST> DEVI bool partialSM(f32x16& p0, f32x16& p1, float& m_reg, float& alpha) {
;     ...
;     } else { const float d = fmaxf(pmax, 0.f); alpha = __builtin_amdgcn_exp2f(-d); m_reg += d;
; #pragma unroll
;         for (int r = 0; r < 16; ++r) { p0[r] = __builtin_amdgcn_exp2f(p0[r] - d); p1[r] = p1[r] - d; }
;         return true;
;     }
.LBB0_705:
	v_max_f32_e32 v50, v126, v126
	v_max_f32_e32 v66, 0, v50
	v_sub_f32_e32 v50, v98, v66
	v_sub_f32_e32 v51, v99, v66
	v_sub_f32_e32 v52, v100, v66
	v_sub_f32_e32 v53, v101, v66
	v_sub_f32_e32 v54, v102, v66
	v_sub_f32_e32 v55, v103, v66
	v_sub_f32_e32 v56, v104, v66
	v_sub_f32_e32 v57, v105, v66
	v_sub_f32_e32 v58, v106, v66
	v_sub_f32_e32 v59, v107, v66
	v_sub_f32_e32 v60, v108, v66
	v_sub_f32_e32 v61, v109, v66
	v_sub_f32_e32 v62, v110, v66
	v_sub_f32_e32 v63, v111, v66
	v_sub_f32_e32 v64, v112, v66
	v_sub_f32_e32 v65, v113, v66
	v_exp_f32_e64 v208, -v66
	v_add_f32_e32 v209, v203, v66
	v_exp_f32_e32 v50, v50
	v_exp_f32_e32 v51, v51
	v_exp_f32_e32 v52, v52
	v_exp_f32_e32 v53, v53
	v_exp_f32_e32 v54, v54
	v_exp_f32_e32 v55, v55
	v_exp_f32_e32 v56, v56
	v_exp_f32_e32 v57, v57
	v_exp_f32_e32 v58, v58
	v_exp_f32_e32 v59, v59
	v_exp_f32_e32 v60, v60
	v_exp_f32_e32 v61, v61
	v_exp_f32_e32 v62, v62
	v_exp_f32_e32 v63, v63
	v_exp_f32_e32 v64, v64
	v_exp_f32_e32 v65, v65
	v_sub_f32_e32 v97, v97, v66
	v_sub_f32_e32 v96, v96, v66
	v_sub_f32_e32 v95, v95, v66
	v_sub_f32_e32 v94, v94, v66
	v_sub_f32_e32 v93, v93, v66
	v_sub_f32_e32 v92, v92, v66
	v_sub_f32_e32 v91, v91, v66
	v_sub_f32_e32 v90, v90, v66
	v_sub_f32_e32 v89, v89, v66
	v_sub_f32_e32 v88, v88, v66
	v_sub_f32_e32 v87, v87, v66
	v_sub_f32_e32 v86, v86, v66
	v_sub_f32_e32 v85, v85, v66
	v_sub_f32_e32 v84, v84, v66
	v_sub_f32_e32 v83, v83, v66
	v_sub_f32_e32 v82, v82, v66
	v_exp_f32_e32 v82, v82
	v_exp_f32_e32 v83, v83
	v_exp_f32_e32 v84, v84
	v_exp_f32_e32 v85, v85
	v_exp_f32_e32 v86, v86
	v_exp_f32_e32 v87, v87
	v_exp_f32_e32 v88, v88
	v_exp_f32_e32 v89, v89
	v_exp_f32_e32 v90, v90
	v_exp_f32_e32 v91, v91
	v_exp_f32_e32 v92, v92
	v_exp_f32_e32 v93, v93
	v_exp_f32_e32 v94, v94
	v_exp_f32_e32 v95, v95
	v_exp_f32_e32 v96, v96
	v_exp_f32_e32 v97, v97
	s_cbranch_execnz .LBB0_698

; template <bool FIRST> DEVI bool partialSM(f32x16& p0, f32x16& p1, float& m_reg, float& alpha) {
;     float pmax = p0[0];
; #pragma unroll
;     for (int r = 1; r < 16; ++r) pmax = fmaxf(pmax, p0[r]);
; #pragma unroll
;     for (int r = 0; r < 16; ++r) pmax = fmaxf(pmax, p1[r]);
;     { auto rr = __builtin_amdgcn_permlane32_swap(__float_as_uint(pmax), __float_as_uint(pmax), false, false);
;       pmax = fmaxf(__uint_as_float(rr[0]), __uint_as_float(rr[1])); }
;     if (FIRST) { m_reg = pmax; alpha = 1.f;
; #pragma unroll
;         for (int r = 0; r < 16; ++r) { p0[r] = __builtin_amdgcn_exp2f(p0[r] - pmax); p1[r] = p1[r] - pmax; }
;         return false;
;     } else if (__builtin_expect(__all(pmax <= ATT_THR), 1)) { alpha = 1.f;
; #pragma unroll
;         for (int r = 0; r < 16; ++r) p0[r] = __builtin_amdgcn_exp2f(p0[r]);
;         return false;
;     } else { const float d = fmaxf(pmax, 0.f); alpha = __builtin_amdgcn_exp2f(-d); m_reg += d;
; #pragma unroll
;         for (int r = 0; r < 16; ++r) { p0[r] = __builtin_amdgcn_exp2f(p0[r] - d); p1[r] = p1[r] - d; }
;         return true;
;     }
; }
; DEVI void finishSM(f32x16& p0, f32x16& p1, float alpha, float& l_reg, bf16x8& pa0, bf16x8& pa1, bf16x8& pa2, bf16x8& pa3) {
; #pragma unroll
;     for (int r = 0; r < 16; ++r) p1[r] = __builtin_amdgcn_exp2f(p1[r]);
;     f32x2 s2 = (f32x2){p0[0], p0[1]} + (f32x2){p1[0], p1[1]};
; #pragma unroll
;     for (int r = 2; r < 16; r += 2) s2 += (f32x2){p0[r], p0[r + 1]} + (f32x2){p1[r], p1[r + 1]};
;     float ps = s2[0] + s2[1];
;     { auto rr = __builtin_amdgcn_permlane32_swap(__float_as_uint(ps), __float_as_uint(ps), false, false);
;       ps = __uint_as_float(rr[0]) + __uint_as_float(rr[1]); }
;     l_reg = l_reg * alpha + ps;
;     ...
;     PK4(p0, 0, pa0); PK4(p0, 8, pa1); PK4(p1, 0, pa2); PK4(p1, 8, pa3);
;     ...
; }
; DEVI void qkt(f32x16& p0, f32x16& p1, const char* Kb, const bf16x8 (&qr)[6], int r32, int hi, const f32x16& cinit) {
; #pragma unroll
;     for (int d0 = 0; d0 < 6; ++d0) { const int cb = (d0 * 16 + hi * 8) * 2;
;         const bf16x8 k0 = *(const bf16x8*)(Kb + KSWZ(r32, cb)), k1 = *(const bf16x8*)(Kb + KSWZ(32 + r32, cb));
;         p0 = __builtin_amdgcn_mfma_f32_32x32x16_bf16(k0, qr[d0], d0 == 0 ? cinit : p0, 0, 0, 0);
;         p1 = __builtin_amdgcn_mfma_f32_32x32x16_bf16(k1, qr[d0], d0 == 0 ? cinit : p1, 0, 0, 0); }
; }
.LBB0_2260:
	v_add_u32_e32 v174, s98, v205
	v_exp_f32_e32 v66, v66
	v_exp_f32_e32 v67, v67
	s_waitcnt lgkmcnt(1)
	v_mfma_f32_32x32x16_bf16 v[98:113], v[82:85], v[150:153], v[34:49]
	v_add_u32_e32 v82, s98, v184
	v_add_u32_e32 v83, s98, v185
	ds_read_b128 v[210:213], v82 offset:12288
	ds_read_b128 v[214:217], v82 offset:18432
	ds_read_b128 v[218:221], v83 offset:12288
	ds_read_b128 v[222:225], v83 offset:18432
	v_exp_f32_e32 v68, v68
	v_exp_f32_e32 v69, v69
	v_exp_f32_e32 v70, v70
	v_exp_f32_e32 v71, v71
	s_waitcnt lgkmcnt(4)
	v_mfma_f32_32x32x16_bf16 v[82:97], v[124:127], v[150:153], v[34:49]
	ds_read_b128 v[124:127], v174 offset:12288
	ds_read_b128 v[226:229], v174 offset:18432
	v_exp_f32_e32 v72, v72
	v_exp_f32_e32 v73, v73
	v_exp_f32_e32 v74, v74
	v_exp_f32_e32 v75, v75
	v_exp_f32_e32 v76, v76
	v_exp_f32_e32 v77, v77
	s_waitcnt lgkmcnt(5)
	v_mfma_f32_32x32x16_bf16 v[98:113], v[210:213], v[138:141], v[98:113]
	v_add_u32_e32 v174, s98, v206
	v_exp_f32_e32 v78, v78
	v_exp_f32_e32 v79, v79
	ds_read_b128 v[230:233], v174 offset:12288
	ds_read_b128 v[234:237], v174 offset:18432
	v_exp_f32_e32 v80, v80
	v_exp_f32_e32 v81, v81
	v_add_u32_e32 v174, s98, v207
	s_waitcnt lgkmcnt(6)
	v_mfma_f32_32x32x16_bf16 v[82:97], v[214:217], v[138:141], v[82:97]
	v_add_f32_e64 v214, v50, v66
	v_add_f32_e64 v215, v51, v67
	v_add_f32_e64 v216, v52, v68
	v_add_f32_e64 v217, v53, v69
	v_lshl_add_u32 v203, s71, 14, v115
	v_add_f32_e32 v214, v216, v214
	v_add_f32_e32 v215, v217, v215
	v_add_f32_e32 v216, v54, v70
	v_add_f32_e32 v217, v55, v71
	ds_read_b128 v[210:213], v174 offset:12288
	ds_read_b128 v[238:241], v174 offset:18432
	v_add_f32_e32 v214, v216, v214
	v_add_f32_e32 v215, v217, v215
	s_waitcnt lgkmcnt(7)
	v_mfma_f32_32x32x16_bf16 v[98:113], v[218:221], v[134:137], v[98:113]
	v_add_f32_e64 v216, v56, v72
	v_add_f32_e64 v217, v57, v73
	v_cvt_pk_bf16_f32 v50, v50, v51
	v_cvt_pk_bf16_f32 v51, v52, v53
	v_cvt_pk_bf16_f32 v52, v54, v55
	v_cvt_pk_bf16_f32 v53, v56, v57
	v_cvt_pk_bf16_f32 v54, v58, v59
	v_add_f32_e64 v214, v216, v214
	v_add_f32_e64 v215, v217, v215
	s_waitcnt lgkmcnt(6)
	v_mfma_f32_32x32x16_bf16 v[82:97], v[222:225], v[134:137], v[82:97]
	v_add_f32_e64 v216, v58, v74
	v_add_f32_e64 v217, v59, v75
	v_cvt_pk_bf16_f32 v55, v60, v61
	v_cvt_pk_bf16_f32 v56, v62, v63
	v_cvt_pk_bf16_f32 v57, v64, v65
	v_cvt_pk_bf16_f32 v58, v66, v67
	v_cvt_pk_bf16_f32 v59, v68, v69
	v_add_f32_e64 v214, v216, v214
	v_add_f32_e64 v215, v217, v215
	s_waitcnt lgkmcnt(5)
	v_mfma_f32_32x32x16_bf16 v[98:113], v[124:127], v[130:133], v[98:113]
	v_add_f32_e64 v216, v60, v76
	v_add_f32_e64 v217, v61, v77
	v_add_f32_e64 v126, v62, v78
	v_add_f32_e64 v127, v63, v79
	v_add_f32_e64 v124, v216, v214
	v_add_f32_e64 v125, v217, v215
	v_cvt_pk_bf16_f32 v60, v70, v71
	v_cvt_pk_bf16_f32 v61, v72, v73
	v_cvt_pk_bf16_f32 v62, v74, v75
	v_cvt_pk_bf16_f32 v63, v76, v77
	s_waitcnt lgkmcnt(4)
	v_mfma_f32_32x32x16_bf16 v[82:97], v[226:229], v[130:133], v[82:97]
	v_add_f32_e64 v124, v126, v124
	v_add_f32_e64 v125, v127, v125
	v_add_f32_e64 v126, v64, v80
	v_add_f32_e64 v127, v65, v81
	v_cvt_pk_bf16_f32 v64, v78, v79
	v_cvt_pk_bf16_f32 v65, v80, v81
	ds_read_b64_tr_b16 v[66:67], v203 offset:0
	ds_read_b64_tr_b16 v[68:69], v203 offset:0x400
	ds_read_b64_tr_b16 v[70:71], v203 offset:0x800
	s_waitcnt lgkmcnt(6)
	v_mfma_f32_32x32x16_bf16 v[98:113], v[230:233], v[146:149], v[98:113]
	ds_read_b64_tr_b16 v[72:73], v203 offset:0xc00
	ds_read_b64_tr_b16 v[74:75], v203 offset:0x1000
	ds_read_b64_tr_b16 v[76:77], v203 offset:0x1400
	ds_read_b64_tr_b16 v[78:79], v203 offset:0x1800
	ds_read_b64_tr_b16 v[80:81], v203 offset:0x1c00
	v_add_f32_e64 v124, v126, v124
	v_add_f32_e64 v125, v127, v125
	s_waitcnt lgkmcnt(10)
	v_mfma_f32_32x32x16_bf16 v[82:97], v[234:237], v[146:149], v[82:97]
	v_add_f32_e32 v124, v124, v125
	s_nop 0
	v_mov_b32_e32 v125, v124
	s_nop 1
	v_permlane32_swap_b32_e32 v124, v125
	s_waitcnt lgkmcnt(9)
	v_mfma_f32_32x32x16_bf16 v[98:113], v[210:213], v[142:145], v[98:113]
	ds_read_b64_tr_b16 v[210:211], v203 offset:0x200
	ds_read_b64_tr_b16 v[212:213], v203 offset:0x600
	ds_read_b64_tr_b16 v[214:215], v203 offset:0xa00
	ds_read_b64_tr_b16 v[216:217], v203 offset:0xe00
	ds_read_b64_tr_b16 v[218:219], v203 offset:0x1200
	ds_read_b64_tr_b16 v[220:221], v203 offset:0x1600
	ds_read_b64_tr_b16 v[222:223], v203 offset:0x1a00
	s_waitcnt lgkmcnt(15)
	v_mfma_f32_32x32x16_bf16 v[82:97], v[238:241], v[142:145], v[82:97]
	ds_read_b64_tr_b16 v[224:225], v203 offset:0x1e00
	s_waitcnt lgkmcnt(14)
	v_mfma_f32_32x32x16_bf16 v[18:33], v[50:53], v[66:69], v[18:33]
	s_waitcnt lgkmcnt(6)
	v_mfma_f32_32x32x16_bf16 v[2:17], v[50:53], v[210:213], v[2:17]
	s_nop 8
	v_max_f32_e32 v249, v99, v99
	v_max_f32_e32 v250, v98, v98
	v_max_f32_e32 v249, v250, v249
	v_max3_f32 v249, v249, v100, v101
	v_max3_f32 v249, v249, v102, v103
	v_max3_f32 v251, v249, v104, v105
	v_max3_f32 v251, v251, v106, v107
	v_exp_f32_e32 v50, v98
	v_exp_f32_e32 v51, v99
	v_exp_f32_e32 v52, v100
	v_exp_f32_e32 v53, v101
	v_mfma_f32_32x32x16_bf16 v[18:33], v[54:57], v[70:73], v[18:33]
	s_waitcnt lgkmcnt(4)
	v_mfma_f32_32x32x16_bf16 v[2:17], v[54:57], v[214:217], v[2:17]
	v_max3_f32 v251, v251, v108, v109
	v_max3_f32 v251, v251, v110, v111
	v_max3_f32 v251, v251, v112, v113
	v_max3_f32 v251, v251, v82, v83
	v_max3_f32 v251, v251, v84, v85
	v_max3_f32 v251, v251, v86, v87
	v_max3_f32 v251, v251, v88, v89
	v_exp_f32_e32 v54, v102
	v_exp_f32_e32 v55, v103
	v_exp_f32_e32 v56, v104
	v_exp_f32_e32 v57, v105
	v_mfma_f32_32x32x16_bf16 v[18:33], v[58:61], v[74:77], v[18:33]
	s_waitcnt lgkmcnt(2)
	v_mfma_f32_32x32x16_bf16 v[2:17], v[58:61], v[218:221], v[2:17]
	v_max3_f32 v251, v251, v90, v91
	v_max3_f32 v251, v251, v92, v93
	v_max3_f32 v251, v251, v94, v95
	v_max3_f32 v251, v251, v96, v97
	v_mov_b32_e32 v252, v251
	s_nop 1
	v_permlane32_swap_b32_e32 v251, v252
	v_exp_f32_e32 v58, v106
	v_exp_f32_e32 v59, v107
	v_exp_f32_e32 v60, v108
	v_exp_f32_e32 v61, v109
	v_mfma_f32_32x32x16_bf16 v[18:33], v[62:65], v[78:81], v[18:33]
	s_waitcnt lgkmcnt(0)
	v_mfma_f32_32x32x16_bf16 v[2:17], v[62:65], v[222:225], v[2:17]
	v_exp_f32_e32 v62, v110
	v_exp_f32_e32 v63, v111
	v_exp_f32_e32 v64, v112
	v_exp_f32_e32 v65, v113
	v_max_f32_e32 v252, v252, v252
	v_max_f32_e32 v251, v251, v251
	v_max_f32_e32 v126, v251, v252
	v_cmp_ge_f32_e32 vcc, s80, v126
	s_cmp_lg_u64 vcc, exec
	s_cselect_b64 s[6:7], -1, 0
	s_cbranch_scc1 .LBB0_2269
	v_mov_b32_e32 v209, 1.0
	v_mov_b32_e32 v210, v204
	v_exp_f32_e32 v82, v82
	v_exp_f32_e32 v83, v83
	v_exp_f32_e32 v84, v84
	v_exp_f32_e32 v85, v85
	v_exp_f32_e32 v86, v86
	v_exp_f32_e32 v87, v87
	v_exp_f32_e32 v88, v88
	v_exp_f32_e32 v89, v89
	v_exp_f32_e32 v90, v90
	v_exp_f32_e32 v91, v91
	v_exp_f32_e32 v92, v92
	v_exp_f32_e32 v93, v93
	v_exp_f32_e32 v94, v94
	v_exp_f32_e32 v95, v95
	v_exp_f32_e32 v96, v96
	v_exp_f32_e32 v97, v97
	s_branch .LBB0_2263

; template <bool FIRST> DEVI bool partialSM(f32x16& p0, f32x16& p1, float& m_reg, float& alpha) {
;     float pmax = p0[0];
; #pragma unroll
;     for (int r = 1; r < 16; ++r) pmax = fmaxf(pmax, p0[r]);
; #pragma unroll
;     for (int r = 0; r < 16; ++r) pmax = fmaxf(pmax, p1[r]);
;     { auto rr = __builtin_amdgcn_permlane32_swap(__float_as_uint(pmax), __float_as_uint(pmax), false, false);
;       pmax = fmaxf(__uint_as_float(rr[0]), __uint_as_float(rr[1])); }
;     if (FIRST) { m_reg = pmax; alpha = 1.f;
; #pragma unroll
;         for (int r = 0; r < 16; ++r) { p0[r] = __builtin_amdgcn_exp2f(p0[r] - pmax); p1[r] = p1[r] - pmax; }
;         return false;
;     } else if (__builtin_expect(__all(pmax <= ATT_THR), 1)) { alpha = 1.f;
; #pragma unroll
;         for (int r = 0; r < 16; ++r) p0[r] = __builtin_amdgcn_exp2f(p0[r]);
;         return false;
;     } else { const float d = fmaxf(pmax, 0.f); alpha = __builtin_amdgcn_exp2f(-d); m_reg += d;
; #pragma unroll
;         for (int r = 0; r < 16; ++r) { p0[r] = __builtin_amdgcn_exp2f(p0[r] - d); p1[r] = p1[r] - d; }
;         return true;
;     }
; }
; DEVI void finishSM(f32x16& p0, f32x16& p1, float alpha, float& l_reg, bf16x8& pa0, bf16x8& pa1, bf16x8& pa2, bf16x8& pa3) {
; #pragma unroll
;     for (int r = 0; r < 16; ++r) p1[r] = __builtin_amdgcn_exp2f(p1[r]);
;     f32x2 s2 = (f32x2){p0[0], p0[1]} + (f32x2){p1[0], p1[1]};
; #pragma unroll
;     for (int r = 2; r < 16; r += 2) s2 += (f32x2){p0[r], p0[r + 1]} + (f32x2){p1[r], p1[r + 1]};
;     float ps = s2[0] + s2[1];
;     { auto rr = __builtin_amdgcn_permlane32_swap(__float_as_uint(ps), __float_as_uint(ps), false, false);
;       ps = __uint_as_float(rr[0]) + __uint_as_float(rr[1]); }
;     l_reg = l_reg * alpha + ps;
;     ...
;     PK4(p0, 0, pa0); PK4(p0, 8, pa1); PK4(p1, 0, pa2); PK4(p1, 8, pa3);
;     ...
; }
; DEVI void qkt(f32x16& p0, f32x16& p1, const char* Kb, const bf16x8 (&qr)[6], int r32, int hi, const f32x16& cinit) {
; #pragma unroll
;     for (int d0 = 0; d0 < 6; ++d0) { const int cb = (d0 * 16 + hi * 8) * 2;
;         const bf16x8 k0 = *(const bf16x8*)(Kb + KSWZ(r32, cb)), k1 = *(const bf16x8*)(Kb + KSWZ(32 + r32, cb));
;         p0 = __builtin_amdgcn_mfma_f32_32x32x16_bf16(k0, qr[d0], d0 == 0 ? cinit : p0, 0, 0, 0);
;         p1 = __builtin_amdgcn_mfma_f32_32x32x16_bf16(k1, qr[d0], d0 == 0 ? cinit : p1, 0, 0, 0); }
; }
.LBB0_2266:
	s_mul_i32 s98, s61, 0x6000
	s_add_i32 s98, s96, s98
	s_lshl_b32 s99, s61, 14
	s_add_i32 s99, s97, s99
	s_mul_i32 s6, s2, 0x6000
	s_add_i32 s6, s6, 0
	v_add_u32_e32 v249, s6, v129
	v_lshl_add_u64 v[250:251], v[118:119], 0, s[12:13]
	s_mov_b32 m0, s98
	s_barrier
	ds_read_b128 v[234:237], v249
	ds_read_b128 v[212:215], v249 offset:6144
	global_load_lds_dwordx4 v[250:251], off
	s_waitcnt lgkmcnt(1)
	v_mfma_f32_32x32x16_bf16 v[98:113], v[234:237], v[150:153], v[34:49]
	v_add_u32_e32 v126, s6, v184
	v_lshl_add_u64 v[250:251], v[120:121], 0, s[12:13]
	s_add_i32 m0, s98, 0x2000
	global_load_lds_dwordx4 v[250:251], off
	s_waitcnt lgkmcnt(0)
	v_mfma_f32_32x32x16_bf16 v[66:81], v[212:215], v[150:153], v[34:49]
	ds_read_b128 v[212:215], v126
	ds_read_b128 v[216:219], v126 offset:6144
	v_add_u32_e32 v126, s6, v185
	v_lshl_add_u64 v[250:251], v[122:123], 0, s[12:13]
	s_add_i32 m0, s98, 0x4000
	global_load_lds_dwordx4 v[250:251], off
	s_waitcnt lgkmcnt(1)
	v_mfma_f32_32x32x16_bf16 v[98:113], v[212:215], v[138:141], v[98:113]
	s_mov_b32 m0, s99
	v_lshl_add_u64 v[250:251], v[116:117], 0, s[40:41]
	global_load_lds_dwordx4 v[116:117], off
	s_add_i32 m0, s99, 0x2000
	v_add_u32_e32 v174, 0x2000, v203
	global_load_lds_dwordx4 v[250:251], off
	s_waitcnt lgkmcnt(0)
	v_mfma_f32_32x32x16_bf16 v[66:81], v[216:219], v[138:141], v[66:81]
	ds_read_b128 v[212:215], v126
	ds_read_b128 v[216:219], v126 offset:6144
	v_add_u32_e32 v126, s6, v205
	s_waitcnt lgkmcnt(1)
	v_mfma_f32_32x32x16_bf16 v[98:113], v[212:215], v[134:137], v[98:113]
	ds_read_b128 v[212:215], v126
	ds_read_b128 v[220:223], v126 offset:6144
	v_add_u32_e32 v126, s6, v206
	s_waitcnt lgkmcnt(2)
	v_mfma_f32_32x32x16_bf16 v[66:81], v[216:219], v[134:137], v[66:81]
	ds_read_b128 v[216:219], v126
	ds_read_b128 v[224:227], v126 offset:6144
	v_add_u32_e32 v126, s6, v207
	ds_read_b128 v[228:231], v126
	ds_read_b128 v[232:235], v126 offset:6144
	v_add_f32_e32 v126, v50, v82
	v_add_f32_e32 v127, v51, v83
	v_cvt_pk_bf16_f32 v50, v50, v51
	v_cvt_pk_bf16_f32 v51, v52, v53
	s_waitcnt lgkmcnt(5)
	v_mfma_f32_32x32x16_bf16 v[98:113], v[212:215], v[130:133], v[98:113]
	v_add_f32_e64 v212, v52, v84
	v_add_f32_e64 v213, v53, v85
	v_cvt_pk_bf16_f32 v52, v54, v55
	v_cvt_pk_bf16_f32 v53, v56, v57
	v_add_f32_e64 v126, v212, v126
	v_add_f32_e64 v127, v213, v127
	v_add_f32_e64 v212, v54, v86
	v_add_f32_e64 v213, v55, v87
	v_cvt_pk_bf16_f32 v54, v58, v59
	s_waitcnt lgkmcnt(4)
	v_mfma_f32_32x32x16_bf16 v[66:81], v[220:223], v[130:133], v[66:81]
	v_add_f32_e64 v126, v212, v126
	v_add_f32_e64 v127, v213, v127
	v_add_f32_e64 v212, v56, v88
	v_add_f32_e64 v213, v57, v89
	v_cvt_pk_bf16_f32 v55, v60, v61
	v_cvt_pk_bf16_f32 v56, v62, v63
	v_cvt_pk_bf16_f32 v57, v64, v65
	v_add_f32_e64 v126, v212, v126
	v_add_f32_e64 v127, v213, v127
	v_add_f32_e32 v212, v58, v90
	v_add_f32_e32 v213, v59, v91
	v_cvt_pk_bf16_f32 v58, v82, v83
	v_cvt_pk_bf16_f32 v59, v84, v85
	s_waitcnt lgkmcnt(3)
	v_mfma_f32_32x32x16_bf16 v[98:113], v[216:219], v[146:149], v[98:113]
	v_add_f32_e64 v126, v212, v126
	v_add_f32_e64 v127, v213, v127
	v_add_f32_e64 v212, v60, v92
	v_add_f32_e64 v213, v61, v93
	v_cvt_pk_bf16_f32 v60, v86, v87
	v_cvt_pk_bf16_f32 v61, v88, v89
	v_add_f32_e64 v126, v212, v126
	v_add_f32_e64 v127, v213, v127
	v_add_f32_e32 v212, v62, v94
	v_add_f32_e32 v213, v63, v95
	v_cvt_pk_bf16_f32 v62, v90, v91
	v_cvt_pk_bf16_f32 v63, v92, v93
	s_waitcnt lgkmcnt(2)
	v_mfma_f32_32x32x16_bf16 v[66:81], v[224:227], v[146:149], v[66:81]
	v_add_f32_e64 v126, v212, v126
	v_add_f32_e64 v127, v213, v127
	v_add_f32_e64 v212, v64, v96
	v_add_f32_e64 v213, v65, v97
	v_cvt_pk_bf16_f32 v64, v94, v95
	v_cvt_pk_bf16_f32 v65, v96, v97
	ds_read_b64_tr_b16 v[154:155], v174 offset:0
	ds_read_b64_tr_b16 v[156:157], v174 offset:0x400
	ds_read_b64_tr_b16 v[158:159], v174 offset:0x800
	ds_read_b64_tr_b16 v[160:161], v174 offset:0xc00
	ds_read_b64_tr_b16 v[162:163], v174 offset:0x1000
	ds_read_b64_tr_b16 v[164:165], v174 offset:0x1400
	ds_read_b64_tr_b16 v[166:167], v174 offset:0x1800
	ds_read_b64_tr_b16 v[168:169], v174 offset:0x1c00
	v_add_f32_e64 v126, v212, v126
	v_add_f32_e64 v127, v213, v127
	ds_read_b64_tr_b16 v[212:213], v174 offset:0x200
	ds_read_b64_tr_b16 v[214:215], v174 offset:0x600
	ds_read_b64_tr_b16 v[216:217], v174 offset:0xa00
	s_waitcnt lgkmcnt(12)
	v_mfma_f32_32x32x16_bf16 v[98:113], v[228:231], v[142:145], v[98:113]
	ds_read_b64_tr_b16 v[218:219], v174 offset:0xe00
	ds_read_b64_tr_b16 v[220:221], v174 offset:0x1200
	ds_read_b64_tr_b16 v[222:223], v174 offset:0x1600
	ds_read_b64_tr_b16 v[224:225], v174 offset:0x1a00
	ds_read_b64_tr_b16 v[226:227], v174 offset:0x1e00
	v_add_f32_e32 v126, v126, v127
	s_waitcnt lgkmcnt(15)
	v_mfma_f32_32x32x16_bf16 v[66:81], v[232:235], v[142:145], v[66:81]
	v_mov_b32_e32 v127, v126
	s_nop 1
	v_permlane32_swap_b32_e32 v126, v127
	s_waitcnt lgkmcnt(14)
	v_mfma_f32_32x32x16_bf16 v[18:33], v[50:53], v[154:157], v[18:33]
	s_waitcnt lgkmcnt(6)
	v_mfma_f32_32x32x16_bf16 v[2:17], v[50:53], v[212:215], v[2:17]
	s_nop 4
	v_max_f32_e32 v249, v99, v99
	v_max_f32_e32 v250, v98, v98
	v_max_f32_e32 v249, v250, v249
	v_max3_f32 v249, v249, v100, v101
	v_max3_f32 v249, v249, v102, v103
	v_max3_f32 v251, v249, v104, v105
	v_max3_f32 v251, v251, v106, v107
	v_exp_f32_e32 v50, v98
	v_exp_f32_e32 v51, v99
	v_exp_f32_e32 v52, v100
	v_exp_f32_e32 v53, v101
	v_mfma_f32_32x32x16_bf16 v[18:33], v[54:57], v[158:161], v[18:33]
	s_waitcnt lgkmcnt(4)
	v_mfma_f32_32x32x16_bf16 v[2:17], v[54:57], v[216:219], v[2:17]
	v_max3_f32 v251, v251, v108, v109
	v_max3_f32 v251, v251, v110, v111
	v_max3_f32 v251, v251, v112, v113
	v_max3_f32 v251, v251, v66, v67
	v_max3_f32 v251, v251, v68, v69
	v_max3_f32 v251, v251, v70, v71
	v_max3_f32 v251, v251, v72, v73
	v_exp_f32_e32 v54, v102
	v_exp_f32_e32 v55, v103
	v_exp_f32_e32 v56, v104
	v_exp_f32_e32 v57, v105
	v_mfma_f32_32x32x16_bf16 v[18:33], v[58:61], v[162:165], v[18:33]
	s_waitcnt lgkmcnt(2)
	v_mfma_f32_32x32x16_bf16 v[2:17], v[58:61], v[220:223], v[2:17]
	v_max3_f32 v251, v251, v74, v75
	v_max3_f32 v251, v251, v76, v77
	v_max3_f32 v251, v251, v78, v79
	v_max3_f32 v251, v251, v80, v81
	v_mov_b32_e32 v252, v251
	s_nop 1
	v_permlane32_swap_b32_e32 v251, v252
	v_exp_f32_e32 v58, v106
	v_exp_f32_e32 v59, v107
	v_exp_f32_e32 v60, v108
	v_exp_f32_e32 v61, v109
	v_mfma_f32_32x32x16_bf16 v[18:33], v[62:65], v[166:169], v[18:33]
	s_waitcnt lgkmcnt(0)
	v_mfma_f32_32x32x16_bf16 v[2:17], v[62:65], v[224:227], v[2:17]
	v_exp_f32_e32 v62, v110
	v_exp_f32_e32 v63, v111
	v_exp_f32_e32 v64, v112
	v_exp_f32_e32 v65, v113
	v_max_f32_e32 v252, v252, v252
	v_max_f32_e32 v251, v251, v251
	v_max_f32_e32 v174, v251, v252
	v_cmp_ge_f32_e32 vcc, s80, v174
	s_cmp_lg_u64 vcc, exec
	s_cselect_b64 s[6:7], -1, 0
	s_cbranch_scc1 .LBB0_2275
	v_mov_b32_e32 v203, 1.0
	v_mov_b32_e32 v204, v210
	s_branch .LBB0_2280

; template <bool FIRST> DEVI bool partialSM(f32x16& p0, f32x16& p1, float& m_reg, float& alpha) {
;     ...
;     } else { const float d = fmaxf(pmax, 0.f); alpha = __builtin_amdgcn_exp2f(-d); m_reg += d;
; #pragma unroll
;         for (int r = 0; r < 16; ++r) { p0[r] = __builtin_amdgcn_exp2f(p0[r] - d); p1[r] = p1[r] - d; }
;         return true;
;     }
.LBB0_2269:
	v_max_f32_e32 v50, v126, v126
	v_max_f32_e32 v66, 0, v50
	v_sub_f32_e32 v50, v98, v66
	v_sub_f32_e32 v51, v99, v66
	v_sub_f32_e32 v52, v100, v66
	v_sub_f32_e32 v53, v101, v66
	v_sub_f32_e32 v54, v102, v66
	v_sub_f32_e32 v55, v103, v66
	v_sub_f32_e32 v56, v104, v66
	v_sub_f32_e32 v57, v105, v66
	v_sub_f32_e32 v58, v106, v66
	v_sub_f32_e32 v59, v107, v66
	v_sub_f32_e32 v60, v108, v66
	v_sub_f32_e32 v61, v109, v66
	v_sub_f32_e32 v62, v110, v66
	v_sub_f32_e32 v63, v111, v66
	v_sub_f32_e32 v64, v112, v66
	v_sub_f32_e32 v65, v113, v66
	v_exp_f32_e64 v209, -v66
	v_add_f32_e32 v210, v204, v66
	v_exp_f32_e32 v50, v50
	v_exp_f32_e32 v51, v51
	v_exp_f32_e32 v52, v52
	v_exp_f32_e32 v53, v53
	v_exp_f32_e32 v54, v54
	v_exp_f32_e32 v55, v55
	v_exp_f32_e32 v56, v56
	v_exp_f32_e32 v57, v57
	v_exp_f32_e32 v58, v58
	v_exp_f32_e32 v59, v59
	v_exp_f32_e32 v60, v60
	v_exp_f32_e32 v61, v61
	v_exp_f32_e32 v62, v62
	v_exp_f32_e32 v63, v63
	v_exp_f32_e32 v64, v64
	v_exp_f32_e32 v65, v65
	v_sub_f32_e32 v97, v97, v66
	v_sub_f32_e32 v96, v96, v66
	v_sub_f32_e32 v95, v95, v66
	v_sub_f32_e32 v94, v94, v66
	v_sub_f32_e32 v93, v93, v66
	v_sub_f32_e32 v92, v92, v66
	v_sub_f32_e32 v91, v91, v66
	v_sub_f32_e32 v90, v90, v66
	v_sub_f32_e32 v89, v89, v66
	v_sub_f32_e32 v88, v88, v66
	v_sub_f32_e32 v87, v87, v66
	v_sub_f32_e32 v86, v86, v66
	v_sub_f32_e32 v85, v85, v66
	v_sub_f32_e32 v84, v84, v66
	v_sub_f32_e32 v83, v83, v66
	v_sub_f32_e32 v82, v82, v66
	v_exp_f32_e32 v82, v82
	v_exp_f32_e32 v83, v83
	v_exp_f32_e32 v84, v84
	v_exp_f32_e32 v85, v85
	v_exp_f32_e32 v86, v86
	v_exp_f32_e32 v87, v87
	v_exp_f32_e32 v88, v88
	v_exp_f32_e32 v89, v89
	v_exp_f32_e32 v90, v90
	v_exp_f32_e32 v91, v91
	v_exp_f32_e32 v92, v92
	v_exp_f32_e32 v93, v93
	v_exp_f32_e32 v94, v94
	v_exp_f32_e32 v95, v95
	v_exp_f32_e32 v96, v96
	v_exp_f32_e32 v97, v97
	s_cbranch_execnz .LBB0_2262
